# v50 with the next-layer weight-conversion split moved from 10240/4224 to 11264/3200 items (upper half of the grid takes more)
# speedup vs baseline: 1.0030x; 1.0015x over previous
; #define LAS __attribute__((address_space(3)))
; __device__ __forceinline__ int opaque_tid() { int t = threadIdx.x; asm volatile("" : "+v"(t)); return t; }
;     __device__ __forceinline__ bool next(int i, Unit& u) const {
;         const long L = (long)i * G + c; if (L >= nwg) return false;
;         int wgid = (int)L; { const int q = nwg / NXCD, r = nwg % NXCD, xcd = wgid % NXCD, off = wgid / NXCD; wgid = (xcd < r ? xcd * (q + 1) : r * (q + 1) + (xcd - r) * q) + off; }
;         const int nig = WGM * nN, gid = wgid / nig, fm = gid * WGM, gsz = (nM - fm) < WGM ? (nM - fm) : WGM;
;         u.pm = fm + ((wgid % nig) % gsz); u.pn = (wgid % nig) / gsz; u.e = 0; u.rows = 256;
;         u.a = A + (size_t)u.pm * tstepA; u.b = Bt + (size_t)u.pn * tstep; return true;
; __device__ __forceinline__ void pj_mfma(const Args& a, LAS unsigned char* lds, int layer) {
;     pg8::DenseOrder So; So.init(a.ws + WS_ACT, a.ws + WS_WIN + (size_t)layer * 3328 * D * 2, NTOK, 3328, D, gridDim.x, blockIdx.x);
;     LAS float* gl = (LAS float*)(lds + SEG_OFF + 256);
;     { const int t_ = opaque_tid(); if (t_ < 256) { const int w = t_ >> 6, i = t_ & 63; const float* gp_ = w == 0 ? a.in[I_QGF] : w == 1 ? a.in[I_KGF] : w == 2 ? a.in[I_QGD] : a.in[I_KGD]; gl[t_] = gp_[layer * 64 + i]; } }
;     __syncthreads();
;     EpiProj E{(bf16_t*)(a.ws + WS_PROJ), gl};
;     pg8::gemm_phase<EpiProj, pg8::DenseOrder>(lds, D, So, E);
;     if ((int)blockIdx.x >= (int)gridDim.x - 32) cumsum_unit(a, lds, blockIdx.x - (gridDim.x - 32));
;     if (layer + 1 < NL) { __syncthreads(); constexpr int I_SPLIT = 10240;
;         const int half = gridDim.x / 2; const bool upper = (int)blockIdx.x >= half;
;         p0_prep(a, lds, layer + 1, upper ? half : 0, upper ? (int)gridDim.x - half : half, upper ? 0 : I_SPLIT, upper ? I_SPLIT : (1 << 30)); }
.LBB0_101:
	s_or_b64 exec, exec, s[0:1]
	s_mov_b32 vcc_lo, 0
	s_nop 1
	v_writelane_b32 v254, vcc_lo, 62
	s_nop 1
	s_waitcnt lgkmcnt(0)
	s_barrier
	s_load_dwordx2 s[92:93], s[54:55], 0xa0
	s_load_dwordx16 s[12:27], s[54:55], 0x20
	s_load_dwordx4 s[0:3], s[54:55], 0x90
	s_movk_i32 s5, 0xd1
	s_mov_b32 s67, 0
	s_waitcnt vmcnt(0)
	v_mbcnt_lo_u32_b32 v1, -1, 0
	v_mbcnt_hi_u32_b32 v199, -1, v1
	s_waitcnt lgkmcnt(0)
	v_writelane_b32 v252, s0, 8
	v_and_b32_e32 v240, 64, v199
	s_mul_hi_u32 s85, s77, 0x600
	v_writelane_b32 v252, s1, 9
	v_writelane_b32 v252, s2, 10
	v_writelane_b32 v252, s3, 11
	s_add_u32 s0, s92, 0x100000
	s_addc_u32 s1, s93, 0
	v_writelane_b32 v252, s0, 12
	s_add_u32 s96, s92, 0xbc00000
	s_addc_u32 s97, s93, 0
	v_writelane_b32 v252, s1, 13
	s_lshl_b32 s0, s61, 3
	s_add_u32 s10, s92, 0x180000
	s_addc_u32 s11, s93, 0
	s_add_u32 s80, s92, 0x7c00000
	s_addc_u32 s81, s93, 0
	v_writelane_b32 v252, s0, 14
	s_add_u32 s0, s92, 0xfc00000
	s_addc_u32 s1, s93, 0
	s_add_u32 s50, s92, 0x18c00000
	s_addc_u32 s51, s93, 0
	s_add_u32 s2, s92, 0xa00000
	s_addc_u32 s3, s93, 0
	v_writelane_b32 v252, s2, 15
	s_cmpk_lt_i32 s61, 0x680
	s_mul_i32 s84, s77, 0x600
	v_writelane_b32 v252, s3, 16
	s_cselect_b64 s[2:3], -1, 0
	v_writelane_b32 v252, s2, 17
	v_mov_b32_e32 v35, 0
	v_add_u32_e32 v241, 64, v240
	v_writelane_b32 v252, s3, 18
	s_ashr_i32 s2, s61, 31
	v_writelane_b32 v252, s2, 19
	s_lshr_b32 s2, s2, 29
	s_add_i32 s3, s61, s2
	s_ashr_i32 s2, s3, 3
	s_and_b32 s3, s3, -8
	s_sub_i32 s3, s61, s3
	s_lshl_b32 s4, s3, 6
	s_cmp_lt_i32 s3, 0
	s_cselect_b32 s5, s5, 0xd0
	s_mul_i32 s5, s5, s3
	s_mulk_i32 s3, 0x41
	s_cselect_b32 s3, s3, s4
	s_add_i32 s5, s5, s2
	s_mul_hi_i32 s4, s5, 0x4ec4ec4f
	s_lshr_b32 s6, s4, 31
	s_ashr_i32 s4, s4, 5
	s_add_i32 s4, s4, s6
	s_mul_i32 s6, s4, 0x68
	s_sub_i32 s5, s5, s6
	s_lshl_b32 s7, s4, 3
	s_bfe_i32 s4, s5, 0x80000
	s_bfe_u32 s4, s4, 0x3000c
	s_add_i32 s6, s5, s4
	s_bfe_i32 s4, s6, 0x80000
	s_and_b32 s6, s6, 0xf8
	s_sub_i32 s5, s5, s6
	s_sext_i32_i16 s8, s4
	s_sext_i32_i8 s5, s5
	s_add_i32 s28, s7, s5
	s_ashr_i32 s5, s8, 3
	v_writelane_b32 v252, s5, 20
	s_mov_b32 s6, s28
	s_ashr_i32 s29, s28, 31
	v_writelane_b32 v252, s6, 21
	s_lshr_b32 s4, s8, 3
	v_xor_b32_e32 v236, 16, v199
	v_writelane_b32 v252, s7, 22
	s_lshl_b64 s[6:7], s[28:29], 19
	s_add_u32 s6, s80, s6
	s_addc_u32 s7, s81, s7
	v_writelane_b32 v252, s6, 23
	s_bfe_i64 s[4:5], s[4:5], 0x100000
	s_lshl_b64 s[4:5], s[4:5], 19
	v_writelane_b32 v252, s7, 24
	v_writelane_b32 v252, s4, 25
	v_xor_b32_e32 v237, 32, v199
	v_mov_b32_e32 v238, 1
	v_writelane_b32 v252, s5, 26
	s_ashr_i32 s4, s77, 31
	v_writelane_b32 v252, s4, 27
	s_sub_i32 s4, s77, 32
	s_cmp_ge_i32 s61, s4
	s_cselect_b64 s[6:7], -1, 0
	v_writelane_b32 v252, s6, 28
	s_sub_i32 s4, s61, s4
	s_and_b32 s5, s4, 3
	v_writelane_b32 v252, s7, 29
	s_ashr_i32 s6, s4, 2
	s_ashr_i32 s7, s6, 31
	s_lshl_b32 s5, s5, 2
	s_add_u32 s5, s10, s5
	v_writelane_b32 v252, s10, 30
	s_addc_u32 s8, s11, 0
	s_lshl_b64 s[6:7], s[6:7], 16
	s_add_u32 s6, s5, s6
	s_addc_u32 s7, s8, s7
	s_add_u32 s28, s92, 0x200000
	s_addc_u32 s29, s93, 0
	s_ashr_i32 s5, s4, 31
	s_lshl_b64 s[4:5], s[4:5], 14
	v_writelane_b32 v252, s11, 31
	s_add_u32 s4, s28, s4
	v_writelane_b32 v252, s6, 32
	s_addc_u32 s5, s29, s5
	s_lshr_b32 s8, s77, 1
	v_writelane_b32 v252, s7, 33
	s_sub_i32 s9, s77, s8
	v_writelane_b32 v252, s4, 34
	s_cmp_lt_i32 s61, s8
	v_mov_b32_e32 v198, 0x358637bd
	v_writelane_b32 v252, s5, 35
	s_cselect_b64 s[4:5], -1, 0
	s_and_b64 s[6:7], s[4:5], exec
	s_cselect_b32 s6, s8, s9
	s_movk_i32 s7, 0x3880
	s_cselect_b32 s10, 0, s8
	s_cselect_b32 s8, 0x2c00, 0
	s_cselect_b32 s7, s7, 0x2c00
	s_lshl_b32 s6, s6, 3
	v_writelane_b32 v252, s7, 36
	s_cmp_ge_i32 s61, s10
	v_writelane_b32 v252, s6, 37
	s_cselect_b64 s[6:7], -1, 0
	s_or_b64 s[4:5], s[36:37], s[4:5]
	s_load_dwordx8 s[36:43], s[54:55], 0x60
	s_and_b64 s[4:5], s[6:7], s[4:5]
	v_writelane_b32 v252, s4, 38
	v_mov_b32_e32 v201, 1.0
	v_mov_b32_e32 v239, 0x7f800000
	v_writelane_b32 v252, s5, 39
	s_sub_i32 s4, s61, s10
	s_lshl_b32 s4, s4, 3
	s_add_i32 s4, s4, s8
	s_waitcnt lgkmcnt(0)
	s_mov_b64 s[8:9], s[40:41]
	v_writelane_b32 v252, s4, 40
	s_add_u32 s6, s38, 0x400000
	s_mov_b64 s[10:11], s[42:43]
	s_mov_b64 s[4:5], s[36:37]
	v_writelane_b32 v252, s4, 41
	v_mov_b32_e32 v202, 0x3f317218
	v_mov_b32_e32 v242, 0xff800000
	v_writelane_b32 v252, s5, 42
	v_writelane_b32 v252, s6, 43
	v_writelane_b32 v252, s7, 44
	v_writelane_b32 v252, s8, 45
	v_writelane_b32 v252, s9, 46
	v_writelane_b32 v252, s10, 47
	v_writelane_b32 v252, s11, 48
	s_addc_u32 s7, s39, 0
	v_writelane_b32 v252, s6, 49
	s_add_u32 s4, s16, 0xd04000
	s_movk_i32 s74, 0x1ff
	v_writelane_b32 v252, s7, 50
	v_writelane_b32 v252, s12, 51
	s_addc_u32 s5, s17, 0
	s_mov_b32 s76, 0x800000
	v_writelane_b32 v255, s25, 0
	v_writelane_b32 v255, s26, 1
	v_writelane_b32 v255, s27, 2
	v_writelane_b32 v255, s4, 3
	v_writelane_b32 v252, s13, 52
	v_writelane_b32 v252, s14, 53
	v_writelane_b32 v255, s5, 4
	s_add_u32 s4, s92, 0x5b00000
	s_addc_u32 s5, s93, 0
	v_writelane_b32 v255, s4, 5
	v_writelane_b32 v252, s15, 54
	v_writelane_b32 v252, s16, 55
	v_writelane_b32 v255, s5, 6
	s_add_u32 s4, s92, 0x1b00000
	s_addc_u32 s5, s93, 0
	s_add_u32 s82, s92, 0x700000
	v_writelane_b32 v255, s4, 7
	s_addc_u32 s83, s93, 0
	v_writelane_b32 v252, s17, 56
	v_writelane_b32 v255, s5, 8
	s_add_u32 s4, s92, 0x14000
	v_writelane_b32 v255, s4, 9
	s_addc_u32 s4, s93, 0
	s_add_i32 s6, s61, 0x900
	s_cmpk_lt_i32 s61, 0x200
	v_writelane_b32 v255, s4, 10
	s_cselect_b64 s[4:5], -1, 0
	v_writelane_b32 v255, s4, 11
	v_writelane_b32 v252, s18, 57
	v_writelane_b32 v252, s19, 58
	v_writelane_b32 v255, s5, 12
;     ...
;         if (u < AT_NFOX) {
;             const int qb = 15 - (u >> 5), bh = u & 31, b = bh >> 2, h = bh & 3, q0 = qb * 256;
;             const size_t rb = (size_t)b * S;
;             const bf16_t* Kb = proj + ((size_t)(4 + h) * NTOK + rb) * 64;
;             const bf16_t* Vb = proj + ((size_t)(8 + h) * NTOK + rb) * 64;
;             const float* cum = cumall + (size_t)bh * S;
;             const int jhi = 4 * qb + 3;
;             fox_cr = cum[q0]; fox_cv = cum[64 * (lane <= jhi ? lane : jhi) + 63]; fox_cq = cum[q0 + 32 * wid + r32];
;             if (!(dbg & 1)) { FOX_ISSUE(0); FOX_ISSUE(1); FOX_ISSUE(2); }
;             const bf16_t* Q = proj + ((size_t)(0 + h) * NTOK + rb + q0 + 32 * wid + r32) * 64;
; #pragma unroll
;             for (int d0 = 0; d0 < 4; ++d0) qr[d0] = *(const bf16x8*)(Q + d0 * 16 + hi * 8);
;         } else if (u < AT_NFOX + AT_NDIL) {
;             const int v2 = u - AT_NFOX, bh = v2 % 48, rest = v2 / 48, b = bh / 6, h = bh % 6, p = rest >> 4, x = rest & 15;
;             const int dil = p == 0 ? 1 : p == 1 ? 4 : 16, res = x % dil, nb2 = x / dil;
;             const size_t rb = (size_t)b * S;
;             const bf16_t* Kb = proj + ((size_t)(22 + h) * NTOK + rb) * 64;
;             const bf16_t* Vb = proj + ((size_t)(28 + h) * NTOK + rb) * 64;
;             const int mk_base = 256 * nb2 - 128, tt_lo = nb2 == 0 ? 2 : 0;
;             const size_t rs = (size_t)64 * dil;
; #pragma unroll
;     ...
;             if (tid < 256) { const int st = tid - 64; tab[tid] = (st >= 0 && st <= 128) ? relb[t5_bucket(st * dil) * 6 + h] : -INFINITY; }
;             const size_t trow = (size_t)(256 * nb2 + 32 * wid + r32) * dil + res;
;             const bf16_t* Q = proj + ((size_t)(16 + h) * NTOK + rb + trow) * 64;
; #pragma unroll
;             for (int d0 = 0; d0 < 4; ++d0) qr[d0] = *(const bf16x8*)(Q + d0 * 16 + hi * 8);
;         } else {
;             const int v2 = u - AT_NFOX - AT_NDIL, qb = 15 - v2 / 48, bh = v2 % 48, b = bh / 6, h = bh % 6, q0 = qb * 256;
;             const size_t rb = (size_t)b * S;
;             const bf16_t* Kb = proj + ((size_t)(40 + h) * NTOK + rb) * 64;
;             const bf16_t* Vb = proj + ((size_t)(46 + h) * NTOK + rb) * 64;
;             const int jhi = (q0 + 254) >> 6;
;             if (!(dbg & 1)) { SB_ISSUE(0); SB_ISSUE(1); SB_ISSUE(2); }
	s_and_b64 s[4:5], s[4:5], exec
	s_cselect_b32 s13, s61, s6
	s_cmpk_lt_i32 s13, 0xe00
	s_cselect_b64 s[4:5], -1, 0
	v_writelane_b32 v255, s4, 13
	s_cmpk_gt_i32 s13, 0x1ff
	s_mov_b32 s17, s67
	v_writelane_b32 v255, s5, 14
	s_cselect_b64 s[4:5], -1, 0
	v_writelane_b32 v255, s4, 15
	s_cmpk_gt_u32 s13, 0xaff
	v_writelane_b32 v252, s20, 59
	v_writelane_b32 v255, s5, 16
	s_cselect_b64 s[4:5], -1, 0
	v_writelane_b32 v255, s4, 17
	v_writelane_b32 v252, s21, 60
	s_mov_b32 s21, s67
	v_writelane_b32 v255, s5, 18
	s_add_i32 s4, s13, 0xf500
	s_and_b32 s5, s4, 0xffff
	s_mul_i32 s5, s5, 0xaaab
	s_lshr_b32 s5, s5, 21
	s_mul_i32 s6, s5, 48
	s_sub_i32 s4, s4, s6
	s_and_b32 s6, s4, 0xff
	s_mulk_i32 s6, 0xab
	s_bfe_u32 s6, s6, 0x6000a
	s_mul_i32 s7, s6, 6
	s_sub_i32 s4, s4, s7
	s_and_b32 s4, s4, 0xff
	s_lshl_b32 s6, s6, 12
	s_lshl_b32 s4, s4, 15
	s_add_i32 s7, s6, s4
	s_lshl_b32 s7, s7, 7
	s_add_i32 s8, s7, 0xb800000
	s_add_u32 s8, s96, s8
	s_addc_u32 s9, s97, 0
	s_add_i32 s7, s7, 0xa000000
	s_add_u32 s7, s96, s7
	s_addc_u32 s10, s97, 0
	s_lshl_b32 s11, s5, 14
	s_sub_i32 s12, 0x3f000, s11
	s_lshl_b32 s12, s12, 1
	s_add_u32 s14, s7, s12
	s_addc_u32 s15, s10, 0
	v_writelane_b32 v255, s14, 19
	v_writelane_b32 v252, s22, 61
	v_writelane_b32 v252, s23, 62
	v_writelane_b32 v255, s15, 20
	s_add_u32 s14, s8, s12
	s_addc_u32 s15, s9, 0
	s_sub_i32 s12, 0x3e000, s11
	v_writelane_b32 v255, s14, 21
	s_lshl_b32 s12, s12, 1
	v_writelane_b32 v252, s24, 63
	v_writelane_b32 v255, s15, 22
	s_add_u32 s14, s7, s12
	s_addc_u32 s15, s10, 0
	v_writelane_b32 v255, s14, 23
	s_movk_i32 s56, 0x7f
	s_mov_b32 s57, 0xff800000
	v_writelane_b32 v255, s15, 24
	s_add_u32 s14, s8, s12
	s_addc_u32 s15, s9, 0
	s_sub_i32 s11, 0x3d000, s11
	v_writelane_b32 v255, s14, 25
	s_lshl_b32 s11, s11, 1
	s_mov_b32 s65, 0xc2ce8ed0
	v_writelane_b32 v255, s15, 26
	s_add_u32 s14, s7, s11
	s_addc_u32 s15, s10, 0
	s_add_u32 s8, s8, s11
	s_addc_u32 s9, s9, 0
	s_lshl_b32 s5, s5, 8
	s_sub_i32 s4, s4, s5
	s_add_i32 s5, s13, 0xfe00
	s_add_i32 s4, s4, s6
	s_and_b32 s6, s5, 0xffff
	s_mul_i32 s6, s6, 0xaaab
	s_lshr_b32 s7, s6, 21
	s_mul_i32 s7, s7, 48
	s_sub_i32 s5, s5, s7
	v_writelane_b32 v255, s14, 27
	s_and_b32 s7, s5, 0xff
	s_mulk_i32 s7, 0xab
	v_writelane_b32 v255, s15, 28
	v_writelane_b32 v255, s8, 29
	s_bfe_u32 s7, s7, 0x6000a
	s_add_i32 s4, s4, 0x110f00
	v_writelane_b32 v255, s9, 30
	s_mul_i32 s8, s7, 6
	s_sub_i32 s5, s5, s8
	s_and_b32 s5, s5, 0xff
	s_lshl_b32 s7, s7, 12
	s_lshl_b32 s8, s5, 15
	s_add_i32 s7, s7, s8
	v_writelane_b32 v255, s4, 31
	s_bfe_u32 s4, s6, 0x40015
	s_lshl_b32 s6, s7, 7
	s_add_u32 s6, s96, s6
	s_addc_u32 s8, s97, 0
	s_add_u32 s9, s6, 0x5800000
	s_addc_u32 s10, s8, 0
	s_add_u32 s6, s6, 0x7000000
	s_addc_u32 s8, s8, 0
	s_lshl_b32 s11, s4, 7
	s_or_b32 s12, s11, 0x60000
	s_add_u32 s14, s9, s12
	s_addc_u32 s15, s10, 0
	v_writelane_b32 v255, s14, 32
	s_mov_b64 s[44:45], -1
	s_mov_b64 s[86:87], 0x800
	v_writelane_b32 v255, s15, 33
	s_add_u32 s14, s6, s12
	s_addc_u32 s15, s8, 0
	v_writelane_b32 v255, s14, 34
	s_or_b32 s12, s11, 0x40000
	s_mov_b32 s60, 0xbfb8aa3b
	v_writelane_b32 v255, s15, 35
	s_add_u32 s14, s9, s12
	s_addc_u32 s15, s10, 0
	v_writelane_b32 v255, s14, 36
	s_mov_b64 s[88:89], 0x80
	s_mov_b64 s[94:95], 0x100
	v_writelane_b32 v255, s15, 37
	s_add_u32 s14, s6, s12
	s_addc_u32 s15, s8, 0
	v_writelane_b32 v255, s14, 38
	s_or_b32 s12, s11, 0x20000
	s_mov_b32 s62, s67
	v_writelane_b32 v255, s15, 39
	s_add_u32 s14, s9, s12
	s_addc_u32 s15, s10, 0
	v_writelane_b32 v255, s14, 40
	s_nop 1
	v_writelane_b32 v255, s15, 41
	s_add_u32 s14, s6, s12
	s_addc_u32 s15, s8, 0
	v_writelane_b32 v255, s14, 42
	s_nop 1
	v_writelane_b32 v255, s15, 43
	s_add_u32 s14, s9, s11
	s_addc_u32 s15, s10, 0
	v_writelane_b32 v255, s14, 44
	s_add_u32 s10, s6, s11
	s_addc_u32 s11, s8, 0
	v_writelane_b32 v255, s15, 45
	s_lshl_b32 s5, s5, 2
	v_writelane_b32 v255, s10, 46
	s_add_i32 s5, s5, 0
	s_add_i32 s5, s5, 0x21f00
	v_writelane_b32 v255, s11, 47
	v_writelane_b32 v255, s5, 48
	s_ashr_i32 s5, s13, 5
	s_or_b32 s4, s7, s4
	s_sub_i32 s5, 15, s5
	s_lshl_b32 s6, s13, 10
	s_and_b32 s7, s13, 31
	s_and_b32 s6, s6, 0x7000
	s_lshl_b32 s7, s7, 14
	s_or_b32 s14, s4, 0x80000
	s_and_b32 s8, s13, 3
	s_lshl_b32 s16, s5, 8
	s_add_u32 s18, s28, s7
	s_addc_u32 s19, s29, 0
	s_lshl_b32 s7, s5, 2
	v_writelane_b32 v255, s13, 49
	s_or_b32 s20, s7, 3
	s_lshl_b64 s[4:5], s[16:17], 2
	v_writelane_b32 v255, s28, 50
	s_add_u32 s4, s18, s4
	v_writelane_b32 v255, s29, 51
	s_addc_u32 s5, s19, s5
	v_writelane_b32 v255, s4, 52
	s_mov_b32 s15, s67
	s_nop 0
	v_writelane_b32 v255, s5, 53
	s_lshl_b32 s4, s8, 22
	s_lshl_b32 s5, s6, 7
	s_or_b32 s4, s5, s4
	s_add_u32 s4, s96, s4
	s_addc_u32 s5, s97, 0
	s_add_u32 s9, s4, 0x2000000
	s_addc_u32 s10, s5, 0
	s_add_u32 s11, s4, 0x1000000
	s_addc_u32 s12, s5, 0
	s_lshl_b64 s[4:5], s[20:21], 13
	s_add_u32 s22, s11, s4
	s_addc_u32 s23, s12, s5
	v_writelane_b32 v255, s22, 54
	s_add_u32 s4, s9, s4
	s_addc_u32 s5, s10, s5
	v_writelane_b32 v255, s23, 55
	v_writelane_b32 v255, s4, 56
	s_lshl_b32 s66, s20, 6
	s_nop 0
	v_writelane_b32 v255, s5, 57
	s_mov_b32 s4, s20
	v_writelane_b32 v255, s4, 58
	s_nop 1
	v_writelane_b32 v255, s5, 59
	s_lshl_b64 s[4:5], s[66:67], 2
	s_add_u32 s4, s18, s4
	s_addc_u32 s5, s19, s5
	v_writelane_b32 v255, s4, 60
; #define LAS __attribute__((address_space(3)))
; #define FOX_ISSUE(i) do { const int j_ = jhi - (i), bf_ = (i) & 3; dma_kv(lds, bf_, Kb + (size_t)j_ * 4096, Vb + (size_t)j_ * 4096, 64, wid, lane); \
;         glds4(cum + j_ * 64 + lane, (unsigned)__builtin_amdgcn_readfirstlane(l0 + L_CK + bf_ * 256)); } while (0)
;     ...
;     bf16x8 qr[4];
;     float fox_cr = 0.f, fox_cv = 0.f, fox_cq = 0.f;
;     auto prologue = [&](int u) {
;         if (!UNIT_ON(u)) return;
;         int lane = tid & 63; asm volatile("" : "+v"(lane));
;         const int r32 = lane & 31, hi = lane >> 5;
;         if (u < AT_NFOX) {
;             const int qb = 15 - (u >> 5), bh = u & 31, b = bh >> 2, h = bh & 3, q0 = qb * 256;
;             const size_t rb = (size_t)b * S;
;             const bf16_t* Kb = proj + ((size_t)(4 + h) * NTOK + rb) * 64;
;             const bf16_t* Vb = proj + ((size_t)(8 + h) * NTOK + rb) * 64;
;             const float* cum = cumall + (size_t)bh * S;
;             const int jhi = 4 * qb + 3;
;             fox_cr = cum[q0]; fox_cv = cum[64 * (lane <= jhi ? lane : jhi) + 63]; fox_cq = cum[q0 + 32 * wid + r32];
;             if (!(dbg & 1)) { FOX_ISSUE(0); FOX_ISSUE(1); FOX_ISSUE(2); }
;             const bf16_t* Q = proj + ((size_t)(0 + h) * NTOK + rb + q0 + 32 * wid + r32) * 64;
; #pragma unroll
;             for (int d0 = 0; d0 < 4; ++d0) qr[d0] = *(const bf16x8*)(Q + d0 * 16 + hi * 8);
; __device__ __forceinline__ void op_mfma(const Args& a, LAS unsigned char* lds, int layer, bf16_t* outp = nullptr) {
;     pg8::DenseOrder So; So.init(a.ws + WS_ACT, a.ws + WS_WOUT + (size_t)layer * D * D * 2, NTOK, D, D, gridDim.x, blockIdx.x, (size_t)256 * 128);
;     bf16_t* xb = (bf16_t*)(a.ws + WS_XB);
;     EpiOut E{layer == 0 ? a.in[I_X] : nullptr, xb, outp ? outp : xb, (const float*)(a.ws + WS_MOD) + (size_t)layer * NB * 6144 + 2048};
;     pg8::gemm_phase<EpiOut, pg8::DenseOrder>(lds, D, So, E, 128u, (size_t)NTOK * 128);
	s_or_b32 s66, s7, 2
	s_nop 0
	v_writelane_b32 v255, s5, 61
	s_lshl_b64 s[4:5], s[66:67], 13
	s_add_u32 s20, s11, s4
	s_addc_u32 s21, s12, s5
	s_add_u32 s4, s9, s4
	s_addc_u32 s5, s10, s5
	v_writelane_b32 v253, s4, 0
	s_lshl_b32 s66, s66, 6
	v_writelane_b32 v255, s20, 62
	v_writelane_b32 v253, s5, 1
	s_lshl_b64 s[4:5], s[66:67], 2
	s_add_u32 s4, s18, s4
	s_addc_u32 s5, s19, s5
	v_writelane_b32 v253, s4, 2
	s_or_b32 s66, s7, 1
	v_writelane_b32 v255, s21, 63
	v_writelane_b32 v253, s5, 3
	s_lshl_b64 s[4:5], s[66:67], 13
	s_add_u32 s20, s11, s4
	s_addc_u32 s21, s12, s5
	v_writelane_b32 v253, s20, 4
	s_add_u32 s4, s9, s4
	s_addc_u32 s5, s10, s5
	v_writelane_b32 v253, s21, 5
	v_writelane_b32 v253, s4, 6
	s_lshl_b32 s66, s66, 6
	s_mov_b32 s9, s67
	v_writelane_b32 v253, s5, 7
	s_lshl_b64 s[4:5], s[66:67], 2
	s_add_u32 s4, s18, s4
	v_writelane_b32 v253, s18, 8
	s_addc_u32 s5, s19, s5
	s_nop 0
	v_writelane_b32 v253, s19, 9
	v_writelane_b32 v253, s4, 10
	s_nop 1
	v_writelane_b32 v253, s5, 11
	s_lshl_b32 s4, s8, 15
	s_or_b32 s4, s6, s4
	s_mov_b32 s6, s16
	v_writelane_b32 v253, s6, 12
	s_add_i32 s4, s4, s16
	s_mov_b32 s8, s77
	v_writelane_b32 v253, s7, 13
	s_mov_b32 s6, s61
	s_mov_b32 s7, s67
	v_writelane_b32 v253, s4, 14
	s_lshl_b64 s[4:5], s[6:7], 9
	s_lshl_b64 s[70:71], s[8:9], 9
	v_writelane_b32 v253, s4, 15
	s_nop 1
	v_writelane_b32 v253, s5, 16
	s_add_u32 s4, s92, 0x8c00000
	s_addc_u32 s5, s93, 0
	v_writelane_b32 v253, s4, 17
	s_nop 1
	v_writelane_b32 v253, s5, 18
	s_add_u32 s4, s92, 0x1700000
	v_writelane_b32 v253, s4, 19
	s_addc_u32 s4, s93, 0
	v_writelane_b32 v253, s4, 20
	s_add_u32 s4, s92, 0x10000
	v_writelane_b32 v253, s4, 21
	s_addc_u32 s4, s93, 0
	v_writelane_b32 v253, s4, 22
	s_add_u32 s4, s92, 0x300000
	s_addc_u32 s5, s93, 0
	v_writelane_b32 v253, s4, 23
	s_nop 1
	v_writelane_b32 v253, s5, 24
	s_add_u32 s4, s92, 0x500000
	s_addc_u32 s5, s93, 0
	v_writelane_b32 v253, s4, 25
	s_cmpk_lt_i32 s61, 0x100
	s_nop 0
	v_writelane_b32 v253, s5, 26
	s_cselect_b64 s[4:5], -1, 0
	v_writelane_b32 v253, s4, 27
	s_nop 1
	v_writelane_b32 v253, s5, 28
	s_add_u32 s4, s92, 0x14400000
	s_addc_u32 s5, s93, 0
	v_writelane_b32 v253, s4, 29
	s_nop 1
	v_writelane_b32 v253, s5, 30
	s_add_i32 s4, s77, s61
	v_writelane_b32 v253, s4, 31
	s_add_u32 s4, s92, 0x7c00080
	s_addc_u32 s5, s93, 0
	s_add_i32 s2, s3, s2
	s_ashr_i32 s3, s2, 31
	s_lshr_b32 s3, s3, 27
	v_writelane_b32 v253, s4, 32
	s_add_i32 s3, s2, s3
	s_nop 0
	v_writelane_b32 v253, s5, 33
	s_and_b32 s4, s3, 0xffe0
	s_sub_i32 s2, s2, s4
	s_bfe_i32 s4, s2, 0x80000
	s_bfe_u32 s4, s4, 0x3000c
	s_add_i32 s4, s2, s4
	s_and_b32 s5, s4, 0xf8
	s_sub_i32 s2, s2, s5
	s_ashr_i32 s3, s3, 5
	s_bfe_i32 s4, s4, 0x80000
	s_lshl_b32 s3, s3, 3
	s_sext_i32_i16 s4, s4
	s_sext_i32_i8 s2, s2
	s_add_i32 s10, s3, s2
	s_ashr_i32 s2, s4, 3
	v_writelane_b32 v253, s2, 34
	s_lshr_b32 s2, s4, 3
	s_mov_b32 s4, s10
	s_ashr_i32 s11, s10, 31
	v_writelane_b32 v253, s4, 35
	s_nop 1
	v_writelane_b32 v253, s5, 36
	s_lshl_b64 s[4:5], s[10:11], 15
	s_add_u32 s4, s80, s4
	s_addc_u32 s5, s81, s5
	v_writelane_b32 v253, s14, 37
	s_bfe_i64 s[2:3], s[2:3], 0x100000
	s_lshl_b64 s[2:3], s[2:3], 19
	v_writelane_b32 v253, s15, 38
	v_writelane_b32 v253, s2, 39
	s_nop 1
	v_writelane_b32 v253, s3, 40
	s_add_u32 s2, s4, 0x4000
	s_addc_u32 s3, s5, 0
	v_writelane_b32 v253, s2, 41
	s_nop 1
	v_writelane_b32 v253, s3, 42
	s_add_u32 s2, s4, 0x400000
	v_writelane_b32 v253, s4, 43
	s_addc_u32 s3, s5, 0
	s_lshl_b64 s[52:53], s[8:9], 10
	v_writelane_b32 v253, s5, 44
	v_writelane_b32 v253, s2, 45
	s_add_i32 s64, 0, 0x13000
	s_nop 0
	v_writelane_b32 v253, s3, 46
	s_lshl_b32 s2, s61, 7
	v_writelane_b32 v253, s2, 47
	s_lshl_b32 s2, s77, 7
	v_writelane_b32 v253, s2, 48
	s_mul_i32 s2, s77, 0x3000
	v_writelane_b32 v253, s2, 49
	s_add_i32 s2, 0, 0x21c20
	v_writelane_b32 v253, s2, 50
	s_add_i32 s2, 0, 0x21c24
	v_writelane_b32 v253, s2, 51
	s_add_i32 s2, 0, 0x21000
	v_writelane_b32 v253, s2, 52
	s_add_i32 s2, 0, 0x21100
	v_writelane_b32 v253, s2, 53
	s_add_i32 s2, 0, 0x21200
	v_writelane_b32 v253, s2, 54
	s_add_i32 s2, 0, 0x21504
	v_writelane_b32 v253, s2, 55
	s_add_i32 s2, 0, 0x15040
	v_writelane_b32 v253, s2, 56
	s_add_i32 s2, 0, 0x15000
	v_writelane_b32 v253, s2, 57
	s_add_i32 s2, 0, 0x21e80
	v_writelane_b32 v253, s2, 58
	s_add_i32 s2, 0, 0x21e10
	v_writelane_b32 v253, s2, 59
	s_add_i32 s2, 0, 0x21e20
	v_writelane_b32 v253, s2, 60
	s_add_i32 s2, 0, 0x21e30
	v_writelane_b32 v253, s2, 61
	v_writelane_b32 v253, s54, 62
	s_load_dwordx2 s[4:5], s[54:55], 0x0
	s_mov_b32 s3, 0x42b17218
	v_writelane_b32 v253, s55, 63
	s_waitcnt lgkmcnt(0)
	v_writelane_b32 v254, s4, 0
	s_nop 1
	v_writelane_b32 v254, s5, 1
	s_lshl_b64 s[4:5], s[8:9], 13
	v_writelane_b32 v254, s4, 2
	s_nop 1
	v_writelane_b32 v254, s5, 3
	v_writelane_b32 v254, s6, 4
	s_lshl_b64 s[4:5], s[6:7], 12
	s_nop 0
	v_writelane_b32 v254, s7, 5
	v_writelane_b32 v254, s4, 6
	s_nop 1
	v_writelane_b32 v254, s5, 7
	s_lshl_b64 s[4:5], s[8:9], 14
	v_writelane_b32 v254, s4, 8
	s_nop 1
	v_writelane_b32 v254, s5, 9
	v_writelane_b32 v254, s8, 10
	s_lshl_b64 s[4:5], s[8:9], 12
	s_nop 0
	v_writelane_b32 v254, s9, 11
	v_writelane_b32 v254, s4, 12
	s_nop 1
	v_writelane_b32 v254, s5, 13
	v_writelane_b32 v254, s82, 14
	s_nop 1
	v_writelane_b32 v254, s83, 15
	s_branch .LBB0_104
